# v45 + G5 unit header: accumulator zeroing moved between the rowsrc load issue and its vmcnt(0) wait (loads retargeted to spare VGPRs)
# speedup vs baseline: 1.0034x; 1.0034x over previous
; template <class Epi, class Sched, bool ALIGN_EPI = false, bool SP2 = false>
; __device__ __forceinline__ void gemm_phase(PG8_LAS unsigned char* lds, const Gemm g, const Sched& S, const Epi& E, const bool skip_epi = false) {
;     ...
; #pragma unroll
;         for (int a = 0; a < 2; ++a)
; #pragma unroll
;             for (int b = 0; b < 2; ++b)
; #pragma unroll
;                 for (int m = 0; m < 4; ++m)
; #pragma unroll
;                     for (int n = 0; n < 2; ++n) acc[a][b][m][n] = (f32x4){0.f, 0.f, 0.f, 0.f};
;         cur = nxt; cA = nA; cB = nB; ++ui;
.LBB0_1725:
	s_nop 0
	v_cndmask_b32_e64 v2, 0, 1, s[6:7]
	v_cmp_ne_u32_e64 s[4:5], 1, v2
	s_andn2_b64 vcc, exec, s[6:7]
	s_cbranch_vccnz .Lg5_zero
	s_lshl_b32 s29, s28, 8
	v_add_u32_e32 v2, s29, v1
	v_add_u32_e32 v4, s29, v151
	s_bitset1_b32 s29, 7
	v_ashrrev_i32_e32 v3, 31, v2
	v_ashrrev_i32_e32 v5, 31, v4
	v_add_u32_e32 v6, s29, v1
	v_add_u32_e32 v8, s29, v151
	v_lshl_add_u64 v[2:3], v[2:3], 2, s[20:21]
	v_lshl_add_u64 v[4:5], v[4:5], 2, s[20:21]
	v_ashrrev_i32_e32 v7, 31, v6
	v_ashrrev_i32_e32 v9, 31, v8
	v_lshl_add_u64 v[6:7], v[6:7], 2, s[20:21]
	v_lshl_add_u64 v[8:9], v[8:9], 2, s[20:21]
	global_load_dword v229, v[2:3], off
	s_nop 0
	global_load_dword v251, v[4:5], off
	s_nop 0
	global_load_dword v252, v[6:7], off
	global_load_dword v253, v[8:9], off
.Lg5_zero:
	v_mov_b32_e32 v42, 0
	v_mov_b32_e32 v43, v42
	v_mov_b32_e32 v44, v42
	v_mov_b32_e32 v45, v42
	v_mov_b32_e32 v50, v42
	v_mov_b32_e32 v51, v42
	v_mov_b32_e32 v52, v42
	v_mov_b32_e32 v53, v42
	v_mov_b32_e32 v2, v42
	v_mov_b32_e32 v3, v42
	v_mov_b32_e32 v4, v42
	v_mov_b32_e32 v5, v42
	v_mov_b32_e32 v6, v42
	v_mov_b32_e32 v7, v42
	v_mov_b32_e32 v8, v42
	v_mov_b32_e32 v9, v42
	v_mov_b32_e32 v18, v42
	v_mov_b32_e32 v19, v42
	v_mov_b32_e32 v20, v42
	v_mov_b32_e32 v21, v42
	v_mov_b32_e32 v22, v42
	v_mov_b32_e32 v23, v42
	v_mov_b32_e32 v24, v42
	v_mov_b32_e32 v25, v42
	v_mov_b32_e32 v34, v42
	v_mov_b32_e32 v35, v42
	v_mov_b32_e32 v36, v42
	v_mov_b32_e32 v37, v42
	v_mov_b32_e32 v38, v42
	v_mov_b32_e32 v39, v42
	v_mov_b32_e32 v40, v42
	v_mov_b32_e32 v41, v42
	v_mov_b32_e32 v58, v42
	v_mov_b32_e32 v59, v42
	v_mov_b32_e32 v60, v42
	v_mov_b32_e32 v61, v42
	v_mov_b32_e32 v62, v42
	v_mov_b32_e32 v63, v42
	v_mov_b32_e32 v64, v42
	v_mov_b32_e32 v65, v42
	v_mov_b32_e32 v66, v42
	v_mov_b32_e32 v67, v42
	v_mov_b32_e32 v68, v42
	v_mov_b32_e32 v69, v42
	v_mov_b32_e32 v70, v42
	v_mov_b32_e32 v71, v42
	v_mov_b32_e32 v72, v42
	v_mov_b32_e32 v73, v42
	v_mov_b32_e32 v82, v42
	v_mov_b32_e32 v83, v42
	v_mov_b32_e32 v84, v42
	v_mov_b32_e32 v85, v42
	v_mov_b32_e32 v86, v42
	v_mov_b32_e32 v87, v42
	v_mov_b32_e32 v88, v42
	v_mov_b32_e32 v89, v42
	v_mov_b32_e32 v98, v42
	v_mov_b32_e32 v99, v42
	v_mov_b32_e32 v100, v42
	v_mov_b32_e32 v101, v42
	v_mov_b32_e32 v102, v42
	v_mov_b32_e32 v103, v42
	v_mov_b32_e32 v104, v42
	v_mov_b32_e32 v105, v42
	v_mov_b32_e32 v114, v42
	v_mov_b32_e32 v115, v42
	v_mov_b32_e32 v116, v42
	v_mov_b32_e32 v117, v42
	v_mov_b32_e32 v118, v42
	v_mov_b32_e32 v119, v42
	v_mov_b32_e32 v120, v42
	v_mov_b32_e32 v121, v42
	v_mov_b32_e32 v74, v42
	v_mov_b32_e32 v75, v42
	v_mov_b32_e32 v76, v42
	v_mov_b32_e32 v77, v42
	v_mov_b32_e32 v78, v42
	v_mov_b32_e32 v79, v42
	v_mov_b32_e32 v80, v42
	v_mov_b32_e32 v81, v42
	v_mov_b32_e32 v90, v42
	v_mov_b32_e32 v91, v42
	v_mov_b32_e32 v92, v42
	v_mov_b32_e32 v93, v42
	v_mov_b32_e32 v94, v42
	v_mov_b32_e32 v95, v42
	v_mov_b32_e32 v96, v42
	v_mov_b32_e32 v97, v42
	v_mov_b32_e32 v106, v42
	v_mov_b32_e32 v107, v42
	v_mov_b32_e32 v108, v42
	v_mov_b32_e32 v109, v42
	v_mov_b32_e32 v110, v42
	v_mov_b32_e32 v111, v42
	v_mov_b32_e32 v112, v42
	v_mov_b32_e32 v113, v42
	v_mov_b32_e32 v122, v42
	v_mov_b32_e32 v123, v42
	v_mov_b32_e32 v124, v42
	v_mov_b32_e32 v125, v42
	v_mov_b32_e32 v126, v42
	v_mov_b32_e32 v127, v42
	v_mov_b32_e32 v128, v42
	v_mov_b32_e32 v129, v42
	v_mov_b32_e32 v54, v42
	v_mov_b32_e32 v55, v42
	v_mov_b32_e32 v56, v42
	v_mov_b32_e32 v57, v42
	v_mov_b32_e32 v46, v42
	v_mov_b32_e32 v47, v42
	v_mov_b32_e32 v48, v42
	v_mov_b32_e32 v49, v42
	v_mov_b32_e32 v30, v42
	v_mov_b32_e32 v31, v42
	v_mov_b32_e32 v32, v42
	v_mov_b32_e32 v33, v42
	v_mov_b32_e32 v26, v42
	v_mov_b32_e32 v27, v42
	v_mov_b32_e32 v28, v42
	v_mov_b32_e32 v29, v42
	v_mov_b32_e32 v14, v42
	v_mov_b32_e32 v15, v42
	v_mov_b32_e32 v16, v42
	v_mov_b32_e32 v17, v42
	v_mov_b32_e32 v10, v42
	v_mov_b32_e32 v11, v42
	v_mov_b32_e32 v12, v42
	v_mov_b32_e32 v13, v42
	s_andn2_b64 vcc, exec, s[6:7]
	s_cbranch_vccnz .LBB0_1727
	s_waitcnt vmcnt(0)
	v_readfirstlane_b32 s29, v250
	v_lshl_add_u32 v164, v229, 11, v152
	v_lshl_add_u32 v163, v251, 11, v153
	v_lshl_add_u32 v162, v252, 11, v152
	v_lshl_add_u32 v161, v253, 11, v153
	s_mul_i32 s29, s29, 28
	s_add_i32 s30, s29, s30
.LBB0_1727:
	s_ashr_i32 s31, s30, 31
	s_lshl_b64 s[34:35], s[30:31], 19
	v_readlane_b32 s42, v254, 29
	v_readlane_b32 s43, v254, 30
	s_add_u32 s34, s42, s34
	s_addc_u32 s35, s43, s35
	s_and_b64 s[42:43], s[6:7], exec
	s_cselect_b32 s29, s35, s41
	s_cselect_b32 s31, s34, s40
	v_mov_b32_e32 v143, v133
	v_mov_b32_e32 v141, v133
	s_add_u32 s61, s40, 0x100
	v_lshl_add_u64 v[146:147], s[24:25], 0, v[140:141]
	v_lshl_add_u64 v[148:149], s[24:25], 0, v[142:143]
	s_addc_u32 s62, s41, 0
	s_mov_b32 s63, -2
	s_mov_b64 s[40:41], 0
